# attention softmax row maximum by two v_max3 chains (33 ops instead of 74)
# speedup vs baseline: 1.0066x; 1.0066x over previous
.LBB0_705:
	v_max3_f32 v0, v96, v97, v98
	v_max3_f32 v2, v128, v129, v130
	v_max3_f32 v0, v0, v99, v100
	v_max3_f32 v2, v2, v131, v132
	v_max3_f32 v0, v0, v101, v102
	v_max3_f32 v2, v2, v133, v134
	v_max3_f32 v0, v0, v103, v104
	v_max3_f32 v2, v2, v135, v136
	v_max3_f32 v0, v0, v105, v106
	v_max3_f32 v2, v2, v137, v138
	v_max3_f32 v0, v0, v107, v108
	v_max3_f32 v2, v2, v139, v140
	v_max3_f32 v0, v0, v109, v110
	v_max3_f32 v2, v2, v141, v142
	v_max3_f32 v0, v0, v111, v112
	v_max3_f32 v2, v2, v143, v144
	v_max3_f32 v0, v0, v113, v114
	v_max3_f32 v2, v2, v145, v146
	v_max3_f32 v0, v0, v115, v116
	v_max3_f32 v2, v2, v147, v148
	v_max3_f32 v0, v0, v117, v118
	v_max3_f32 v2, v2, v149, v150
	v_max3_f32 v0, v0, v119, v120
	v_max3_f32 v2, v2, v151, v152
	v_max3_f32 v0, v0, v121, v122
	v_max3_f32 v2, v2, v153, v154
	v_max3_f32 v0, v0, v123, v124
	v_max3_f32 v2, v2, v155, v156
	v_max3_f32 v0, v0, v125, v126
	v_max3_f32 v2, v2, v157, v158
	v_max_f32_e32 v0, v0, v127
	v_max_f32_e32 v2, v2, v159
	v_max_f32_e32 v0, v0, v2
	v_mov_b32_e32 v2, v0
	s_nop 1
	v_permlane32_swap_b32_e32 v0, v2
	v_max_f32_e32 v2, v2, v2
	v_max_f32_e32 v0, v0, v0
	v_max_f32_e32 v0, v0, v2
	v_mul_f32_e32 v2, 0x39000000, v0
	v_fma_f32 v0, v0, s60, -v213
	v_cmp_ge_f32_e32 vcc, s61, v0
	s_cmp_eq_u64 vcc, exec
	v_max_f32_e32 v0, v213, v213
	v_max_f32_e32 v0, v0, v2
	s_cselect_b64 vcc, -1, 0
	v_sub_f32_e32 v4, v213, v0
	v_cndmask_b32_e32 v213, v0, v213, vcc
	v_fma_f32 v0, v112, s60, -v213
	v_exp_f32_e32 v22, v0
	v_fma_f32 v0, v96, s60, -v213
	v_exp_f32_e32 v2, v0
	v_fma_f32 v0, v144, s60, -v213
	v_exp_f32_e32 v17, v4
	v_fma_f32 v4, v113, s60, -v213
	v_exp_f32_e32 v3, v0
	v_fma_f32 v0, v128, s60, -v213
	v_exp_f32_e32 v28, v4
	v_fma_f32 v4, v97, s60, -v213
	v_exp_f32_e32 v0, v0
	v_exp_f32_e32 v25, v4
	v_fma_f32 v4, v145, s60, -v213
	v_exp_f32_e32 v5, v4
	v_fma_f32 v4, v129, s60, -v213
	v_exp_f32_e32 v4, v4
	v_add_f32_e32 v6, v2, v22
	v_add_f32_e32 v7, v0, v3
	v_add_f32_e32 v6, v7, v6
	v_add_f32_e32 v8, 0, v6
	v_add_f32_e32 v9, v25, v28
	v_add_f32_e32 v18, v4, v5
	v_fma_f32 v6, v114, s60, -v213
	v_exp_f32_e32 v26, v6
	v_fma_f32 v6, v98, s60, -v213
	v_add_f32_e32 v9, v18, v9
	v_exp_f32_e32 v27, v6
	v_fma_f32 v6, v146, s60, -v213
	v_fma_f32 v7, v130, s60, -v213
	v_add_f32_e32 v18, v9, v8
	v_fma_f32 v8, v115, s60, -v213
	v_exp_f32_e32 v6, v6
	v_exp_f32_e32 v7, v7
	v_exp_f32_e32 v31, v8
	v_fma_f32 v8, v99, s60, -v213
	v_exp_f32_e32 v96, v8
	v_fma_f32 v8, v147, s60, -v213
	v_fma_f32 v9, v131, s60, -v213
	v_exp_f32_e32 v8, v8
	v_exp_f32_e32 v9, v9
	v_add_f32_e32 v19, v27, v26
	v_add_f32_e32 v20, v7, v6
	v_add_f32_e32 v19, v20, v19
	v_fma_f32 v20, v116, s60, -v213
	v_add_f32_e32 v18, v19, v18
	v_add_f32_e32 v19, v96, v31
	v_add_f32_e32 v23, v9, v8
	v_exp_f32_e32 v113, v20
	v_fma_f32 v20, v100, s60, -v213
	v_exp_f32_e32 v112, v20
	v_fma_f32 v20, v148, s60, -v213
	v_add_f32_e32 v19, v23, v19
	v_fma_f32 v23, v117, s60, -v213
	v_exp_f32_e32 v21, v20
	v_fma_f32 v20, v132, s60, -v213
	v_exp_f32_e32 v115, v23
	v_fma_f32 v23, v101, s60, -v213
	v_exp_f32_e32 v20, v20
	v_exp_f32_e32 v114, v23
	v_fma_f32 v23, v149, s60, -v213
	v_exp_f32_e32 v24, v23
	v_fma_f32 v23, v133, s60, -v213
	v_exp_f32_e32 v23, v23
	v_add_f32_e32 v18, v19, v18
	v_add_f32_e32 v19, v112, v113
	v_add_f32_e32 v29, v20, v21
	v_add_f32_e32 v19, v29, v19
	v_fma_f32 v29, v118, s60, -v213
	v_add_f32_e32 v18, v19, v18
	v_add_f32_e32 v19, v114, v115
	v_add_f32_e32 v97, v23, v24
	v_exp_f32_e32 v116, v29
	v_fma_f32 v29, v102, s60, -v213
	v_exp_f32_e32 v117, v29
	v_fma_f32 v29, v150, s60, -v213
	v_fma_f32 v30, v134, s60, -v213
	v_add_f32_e32 v19, v97, v19
	v_fma_f32 v97, v119, s60, -v213
	v_exp_f32_e32 v29, v29
	v_exp_f32_e32 v30, v30
	v_exp_f32_e32 v118, v97
	v_fma_f32 v97, v103, s60, -v213
	v_exp_f32_e32 v119, v97
	v_fma_f32 v97, v151, s60, -v213
	v_fma_f32 v98, v135, s60, -v213
	v_exp_f32_e32 v97, v97
	v_exp_f32_e32 v98, v98
	v_add_f32_e32 v18, v19, v18
	v_add_f32_e32 v19, v117, v116
	v_add_f32_e32 v99, v30, v29
	v_add_f32_e32 v19, v99, v19
	v_fma_f32 v99, v120, s60, -v213
	v_add_f32_e32 v18, v19, v18
	v_add_f32_e32 v19, v119, v118
	v_add_f32_e32 v101, v98, v97
	v_exp_f32_e32 v128, v99
	v_fma_f32 v99, v104, s60, -v213
	v_exp_f32_e32 v120, v99
	v_fma_f32 v99, v152, s60, -v213
	v_add_f32_e32 v19, v101, v19
	v_fma_f32 v101, v121, s60, -v213
	v_exp_f32_e32 v100, v99
	v_fma_f32 v99, v136, s60, -v213
	v_exp_f32_e32 v131, v101
	v_fma_f32 v101, v105, s60, -v213
	v_exp_f32_e32 v99, v99
	v_exp_f32_e32 v129, v101
	v_fma_f32 v101, v153, s60, -v213
	v_exp_f32_e32 v104, v101
	v_fma_f32 v101, v137, s60, -v213
	v_exp_f32_e32 v101, v101
	v_add_f32_e32 v18, v19, v18
	v_add_f32_e32 v19, v120, v128
	v_add_f32_e32 v102, v99, v100
	v_add_f32_e32 v19, v102, v19
	v_fma_f32 v102, v122, s60, -v213
	v_add_f32_e32 v18, v19, v18
	v_add_f32_e32 v19, v129, v131
	v_add_f32_e32 v105, v101, v104
	v_exp_f32_e32 v122, v102
	v_fma_f32 v102, v106, s60, -v213
	v_exp_f32_e32 v130, v102
	v_fma_f32 v102, v154, s60, -v213
	v_fma_f32 v103, v138, s60, -v213
	v_add_f32_e32 v19, v105, v19
	v_fma_f32 v105, v123, s60, -v213
	v_exp_f32_e32 v102, v102
	v_exp_f32_e32 v103, v103
	v_exp_f32_e32 v132, v105
	v_fma_f32 v105, v107, s60, -v213
	v_exp_f32_e32 v133, v105
	v_fma_f32 v105, v155, s60, -v213
	v_fma_f32 v106, v139, s60, -v213
	v_exp_f32_e32 v105, v105
	v_exp_f32_e32 v106, v106
	v_fma_f32 v107, v124, s60, -v213
	v_add_f32_e32 v18, v19, v18
	v_add_f32_e32 v19, v130, v122
	v_add_f32_e32 v121, v103, v102
	v_exp_f32_e32 v135, v107
	v_fma_f32 v107, v108, s60, -v213
	v_add_f32_e32 v19, v121, v19
	v_exp_f32_e32 v134, v107
	v_fma_f32 v107, v156, s60, -v213
	v_add_f32_e32 v18, v19, v18
	v_add_f32_e32 v19, v133, v132
	v_add_f32_e32 v121, v106, v105
	v_exp_f32_e32 v108, v107
	v_fma_f32 v107, v140, s60, -v213
	v_fma_f32 v109, v109, s60, -v213
	v_exp_f32_e32 v107, v107
	v_add_f32_e32 v19, v121, v19
	v_fma_f32 v121, v125, s60, -v213
	v_exp_f32_e32 v125, v109
	v_fma_f32 v109, v157, s60, -v213
	v_exp_f32_e32 v136, v121
	v_exp_f32_e32 v121, v109
	v_fma_f32 v109, v141, s60, -v213
	v_exp_f32_e32 v109, v109
	v_add_f32_e32 v18, v19, v18
	v_add_f32_e32 v19, v134, v135
	v_add_f32_e32 v123, v107, v108
	v_add_f32_e32 v19, v123, v19
	v_fma_f32 v123, v126, s60, -v213
	v_fma_f32 v110, v110, s60, -v213
	v_add_f32_e32 v18, v19, v18
	v_add_f32_e32 v19, v125, v136
	v_add_f32_e32 v124, v109, v121
	v_exp_f32_e32 v126, v123
	v_exp_f32_e32 v137, v110
	v_fma_f32 v110, v158, s60, -v213
	v_fma_f32 v123, v142, s60, -v213
	v_exp_f32_e32 v110, v110
	v_exp_f32_e32 v123, v123
	v_add_f32_e32 v19, v124, v19
	v_fma_f32 v124, v127, s60, -v213
	v_fma_f32 v111, v111, s60, -v213
	v_exp_f32_e32 v127, v124
	v_exp_f32_e32 v138, v111
	v_fma_f32 v111, v159, s60, -v213
	v_fma_f32 v124, v143, s60, -v213
	v_exp_f32_e32 v111, v111
	v_exp_f32_e32 v124, v124
	v_add_f32_e32 v18, v19, v18
	v_add_f32_e32 v19, v137, v126
	v_add_f32_e32 v139, v123, v110
	v_add_f32_e32 v19, v139, v19
	v_add_f32_e32 v18, v19, v18
	v_add_f32_e32 v19, v138, v127
	v_add_f32_e32 v139, v124, v111
	v_add_f32_e32 v19, v139, v19
	v_add_f32_e32 v18, v19, v18
	v_cndmask_b32_e64 v17, v17, 1.0, vcc
	v_mov_b32_e32 v19, v18
	s_nop 1
	v_permlane32_swap_b32_e32 v18, v19
	v_cmp_gt_f32_e32 vcc, 1.0, v17
	s_cbranch_vccz .LBB0_709
	v_mov_b32_e32 v140, v210
	v_mov_b32_e32 v139, v211
	s_nop 0
	v_cmp_eq_u32_e32 vcc, 0, v139
	s_and_saveexec_b64 s[6:7], vcc
	v_lshl_add_u32 v140, v140, 2, s69
	ds_write_b32 v140, v17 offset:128
	s_or_b64 exec, exec, s[6:7]
	v_lshl_add_u32 v139, v139, 4, s69
	s_waitcnt lgkmcnt(0)
	ds_read_b128 v[140:143], v139 offset:224
	ds_read_b128 v[144:147], v139 offset:192
	ds_read_b128 v[148:151], v139 offset:160
	ds_read_b128 v[152:155], v139 offset:128
	s_waitcnt lgkmcnt(3)
	v_pk_mul_f32 v[94:95], v[94:95], v[142:143]
	s_waitcnt lgkmcnt(2)
	v_pk_mul_f32 v[90:91], v[90:91], v[146:147]
	s_waitcnt lgkmcnt(1)
	v_pk_mul_f32 v[86:87], v[86:87], v[150:151]
	s_waitcnt lgkmcnt(0)
	v_pk_mul_f32 v[82:83], v[82:83], v[154:155]
	v_pk_mul_f32 v[92:93], v[92:93], v[140:141]
	v_pk_mul_f32 v[88:89], v[88:89], v[144:145]
	v_pk_mul_f32 v[84:85], v[84:85], v[148:149]
	v_pk_mul_f32 v[80:81], v[80:81], v[152:153]
	v_pk_mul_f32 v[78:79], v[78:79], v[142:143]
	v_pk_mul_f32 v[74:75], v[74:75], v[146:147]
	v_pk_mul_f32 v[70:71], v[70:71], v[150:151]
	v_pk_mul_f32 v[66:67], v[66:67], v[154:155]
	v_pk_mul_f32 v[76:77], v[76:77], v[140:141]
	v_pk_mul_f32 v[72:73], v[72:73], v[144:145]
	v_pk_mul_f32 v[68:69], v[68:69], v[148:149]
	v_pk_mul_f32 v[64:65], v[64:65], v[152:153]
	v_pk_mul_f32 v[46:47], v[46:47], v[142:143]
	v_pk_mul_f32 v[42:43], v[42:43], v[146:147]
	v_pk_mul_f32 v[38:39], v[38:39], v[150:151]
	v_pk_mul_f32 v[34:35], v[34:35], v[154:155]
	v_pk_mul_f32 v[44:45], v[44:45], v[140:141]
	v_pk_mul_f32 v[40:41], v[40:41], v[144:145]
	v_pk_mul_f32 v[36:37], v[36:37], v[148:149]
	v_pk_mul_f32 v[32:33], v[32:33], v[152:153]
	v_pk_mul_f32 v[62:63], v[62:63], v[142:143]
	v_pk_mul_f32 v[58:59], v[58:59], v[146:147]
	v_pk_mul_f32 v[54:55], v[54:55], v[150:151]
	v_pk_mul_f32 v[50:51], v[50:51], v[154:155]
	v_pk_mul_f32 v[60:61], v[60:61], v[140:141]
	v_pk_mul_f32 v[56:57], v[56:57], v[144:145]
	v_pk_mul_f32 v[52:53], v[52:53], v[148:149]
	v_pk_mul_f32 v[48:49], v[48:49], v[152:153]
